# baseline (speedup 1.0000x reference)
.Lmy_noprio:
	s_lshl_b64 s[76:77], s[38:39], 18
	s_waitcnt lgkmcnt(0)
	s_add_u32 s0, s70, s76
	v_bfe_u32 v4, v0, 5, 1
	v_and_b32_e32 v1, 63, v0
	v_writelane_b32 v252, s0, 0
	s_addc_u32 s0, s71, s77
	v_lshlrev_b32_e32 v159, 2, v4
	v_writelane_b32 v252, s0, 1
	v_cmp_gt_u32_e64 s[4:5], 32, v1
	v_sub_u32_e32 v3, v0, v159
	v_mov_b32_e32 v2, 0x3c00
	v_writelane_b32 v252, s4, 2
	v_lshlrev_b32_e32 v3, 2, v3
	v_or_b32_e32 v11, 1, v159
	s_lshl_b32 s40, s33, 16
	v_writelane_b32 v252, s5, 3
	v_cndmask_b32_e64 v2, 0, v2, s[4:5]
	s_lshr_b32 s41, s1, 6
	s_bfe_u32 s5, s2, 0x30003
	v_and_b32_e32 v9, 0x7c, v3
	v_sub_u32_e32 v3, v0, v11
	s_add_u32 s0, s72, s76
	v_lshlrev_b32_e32 v3, 2, v3
	v_or_b32_e32 v166, 2, v159
	v_writelane_b32 v252, s0, 4
	s_addc_u32 s0, s73, s77
	v_and_b32_e32 v12, 0x7c, v3
	v_sub_u32_e32 v3, v0, v166
	v_writelane_b32 v252, s0, 5
	s_lshl_b32 s0, s41, 12
	v_lshlrev_b32_e32 v3, 2, v3
	v_or_b32_e32 v167, 3, v159
	s_lshl_b64 s[2:3], s[38:39], 11
	v_bfe_u32 v5, v0, 4, 2
	s_bfe_u32 s39, s1, 0x20006
	s_add_i32 s0, s0, 0x20000
	v_and_b32_e32 v14, 0x7c, v3
	v_sub_u32_e32 v3, v0, v167
	v_xor_b32_e32 v28, v5, v0
	v_bitop3_b32 v5, v5, v0, 4 bitop3:0x36
	v_writelane_b32 v252, s5, 6
	s_xor_b32 s5, s5, 15
	s_lshl_b32 s48, s39, 5
	v_lshlrev_b32_e32 v3, 2, v3
	v_or_b32_e32 v168, 8, v159
	v_pack_b32_f16 v118, v2, 0
	v_bfe_u32 v2, v0, 3, 3
	v_lshlrev_b32_e32 v28, 4, v28
	v_lshlrev_b32_e32 v5, 4, v5
	s_cmpk_lt_u32 s1, 0x100
	v_and_b32_e32 v16, 0x7c, v3
	v_sub_u32_e32 v3, v0, v168
	v_lshlrev_b32_e32 v27, 7, v2
	v_and_b32_e32 v28, 0x70, v28
	v_and_b32_e32 v5, 0x70, v5
	v_writelane_b32 v252, s5, 7
	s_cselect_b64 s[44:45], -1, 0
	s_lshl_b32 s5, s39, 1
	v_and_b32_e32 v6, 31, v0
	v_lshlrev_b32_e32 v3, 2, v3
	v_or_b32_e32 v169, 9, v159
	v_lshlrev_b32_e32 v2, 12, v2
	v_or_b32_e32 v172, v28, v27
	v_or_b32_e32 v174, v5, v27
	v_lshlrev_b32_e32 v27, 3, v0
	v_writelane_b32 v252, s5, 8
	s_or_b32 s5, s5, 1
	v_and_b32_e32 v18, 0x7c, v3
	v_sub_u32_e32 v3, v0, v169
	v_lshlrev_b32_e32 v26, 9, v4
	v_or_b32_e32 v173, v28, v2
	v_or_b32_e32 v175, v5, v2
	v_and_b32_e32 v28, 0x70, v27
	s_lshl_b32 s6, s5, 10
	v_writelane_b32 v252, s5, 9
	s_lshl_b32 s5, s5, 15
	v_or_b32_e32 v158, s2, v6
	v_lshlrev_b32_e32 v2, 3, v4
	v_lshlrev_b32_e32 v4, 4, v4
	s_movk_i32 s2, 0x60
	v_lshlrev_b32_e32 v3, 2, v3
	v_or_b32_e32 v170, 10, v159
	v_writelane_b32 v252, s5, 10
	v_bitop3_b32 v180, v4, v28, s2 bitop3:0x36
	s_bfe_u32 s2, s41, 0x10001
	v_and_b32_e32 v20, 0x7c, v3
	v_sub_u32_e32 v3, v0, v170
	s_lshl_b32 s50, s39, 11
	v_writelane_b32 v252, s6, 11
	s_or_b32 s2, s2, -6
	v_lshlrev_b32_e32 v3, 2, v3
	v_or_b32_e32 v171, 11, v159
	v_writelane_b32 v252, s2, 12
	s_and_b32 s2, s50, 0x800
	v_and_b32_e32 v22, 0x7c, v3
	v_sub_u32_e32 v3, v0, v171
	v_lshlrev_b32_e32 v29, 4, v1
	s_or_b32 s2, s40, s2
	v_lshlrev_b32_e32 v3, 2, v3
	s_lshl_b32 s49, s39, 16
	s_or_b32 s1, s40, s50
	s_or_b32 s42, s40, s6
	v_mov_b32_e32 v1, s3
	s_or_b32 s3, s50, 0x1000
	v_or_b32_e32 v190, s2, v29
	s_or_b32 s2, s50, 0x1400
	v_and_b32_e32 v24, 0x7c, v3
	v_mov_b32_e32 v3, 0
	v_writelane_b32 v252, s3, 13
	s_cmp_eq_u32 s33, 1
	s_movk_i32 s4, 0x70
	v_mov_b32_e32 v5, v3
	v_writelane_b32 v252, s2, 14
	v_readfirstlane_b32 s100, v190
	s_cselect_b64 s[2:3], -1, 0
	v_lshl_add_u64 v[160:161], s[68:69], 0, v[4:5]
	v_bitop3_b32 v177, v4, v27, s4 bitop3:0x78
	v_bitop3_b32 v178, v4, v28, 32 bitop3:0x36
	v_bitop3_b32 v179, v4, v28, 64 bitop3:0x36
	v_writelane_b32 v252, s2, 15
	v_mov_b32_e32 v4, 2
	v_lshlrev_b32_sdwa v207, v4, v0 dst_sel:DWORD dst_unused:UNUSED_PAD src0_sel:DWORD src1_sel:BYTE_0
	v_writelane_b32 v252, s3, 16
	s_lshl_b32 s2, s38, 7
	v_mov_b32_e32 v4, 0x7ffff81f
	v_bitop3_b32 v0, s2, v4, v0 bitop3:0xc8
	s_and_b32 s2, s2, 0x780
	s_add_u32 s2, s36, s2
	s_addc_u32 s3, s37, 0
	v_lshl_add_u64 v[162:163], s[2:3], 0, v[2:3]
	s_or_b32 s2, s49, 0x8080
	v_writelane_b32 v252, s2, 17
	s_or_b32 s2, s49, 0x80
	s_lshl_b32 s51, s39, 12
	v_writelane_b32 v252, s2, 18
	s_or_b32 s2, s50, 0x2000
	v_writelane_b32 v252, s2, 19
	s_add_u32 s2, s70, 0x400
	v_writelane_b32 v252, s2, 20
	s_addc_u32 s2, s71, 0
	v_writelane_b32 v252, s2, 21
	s_or_b32 s2, s50, 0x4000
	v_writelane_b32 v252, s2, 22
	s_add_u32 s2, s70, 0x4000
	v_writelane_b32 v252, s2, 23
	s_addc_u32 s2, s71, 0
	v_writelane_b32 v252, s2, 24
	s_or_b32 s2, s49, 0x8100
	v_writelane_b32 v252, s2, 25
	s_add_u32 s2, s72, 0x100
	v_writelane_b32 v252, s2, 26
	s_addc_u32 s2, s73, 0
	v_writelane_b32 v252, s2, 27
	v_writelane_b32 v252, s44, 28
	v_cmp_gt_u32_e64 s[52:53], v6, v159
	v_lshlrev_b32_e32 v7, 2, v6
	v_writelane_b32 v252, s45, 29
	v_writelane_b32 v252, s52, 30
	v_lshlrev_b32_e32 v8, 7, v6
	v_or_b32_e32 v10, v9, v8
	v_writelane_b32 v252, s53, 31
	v_writelane_b32 v252, s51, 32
	v_or_b32_e32 v13, v12, v8
	v_or_b32_e32 v15, v14, v8
	v_or_b32_e32 v17, v16, v8
	v_or_b32_e32 v19, v18, v8
	v_or_b32_e32 v21, v20, v8
	v_or_b32_e32 v23, v22, v8
	v_or_b32_e32 v25, v24, v8
	v_or_b32_e32 v176, s40, v8
	v_or3_b32 v181, s0, v26, v7
	v_cmp_gt_u32_e64 s[4:5], v6, v11
	v_or_b32_e32 v182, 16, v159
	v_or_b32_e32 v183, 17, v159
	v_or_b32_e32 v184, 18, v159
	v_or_b32_e32 v185, 19, v159
	v_or_b32_e32 v186, 24, v159
	v_or_b32_e32 v187, 25, v159
	v_or_b32_e32 v188, 26, v159
	v_or_b32_e32 v189, 27, v159
	v_bitop3_b32 v4, v9, 64, v8 bitop3:0x36
	v_bitop3_b32 v5, v12, 64, v8 bitop3:0x36
	v_bitop3_b32 v7, v14, 64, v8 bitop3:0x36
	v_bitop3_b32 v9, v16, 64, v8 bitop3:0x36
	v_bitop3_b32 v11, v18, 64, v8 bitop3:0x36
	v_bitop3_b32 v12, v20, 64, v8 bitop3:0x36
	v_bitop3_b32 v14, v22, 64, v8 bitop3:0x36
	v_bitop3_b32 v8, v24, 64, v8 bitop3:0x36
	v_add_u32_e32 v210, s1, v29
	v_add_u32_e32 v212, s42, v29
	v_writelane_b32 v252, s48, 33
	v_readfirstlane_b32 s101, v210
	v_mov_b32_e32 v119, v3
	v_mov_b32_e32 v120, v3
	v_mov_b32_e32 v121, v3
	v_cmp_gt_u32_e64 s[6:7], v6, v166
	v_cmp_gt_u32_e64 s[8:9], v6, v167
	v_cmp_gt_u32_e64 s[10:11], v6, v168
	v_cmp_gt_u32_e64 s[12:13], v6, v169
	v_cmp_gt_u32_e64 s[14:15], v6, v170
	v_cmp_gt_u32_e64 s[16:17], v6, v171
	v_cmp_gt_u32_e64 s[18:19], v6, v182
	v_cmp_gt_u32_e64 s[20:21], v6, v183
	v_cmp_gt_u32_e64 s[22:23], v6, v184
	v_cmp_gt_u32_e64 s[24:25], v6, v185
	v_cmp_gt_u32_e64 s[26:27], v6, v186
	v_cmp_gt_u32_e64 s[28:29], v6, v187
	v_cmp_gt_u32_e64 s[30:31], v6, v188
	v_cmp_gt_u32_e64 s[34:35], v6, v189
	v_or_b32_e32 v191, 32, v159
	v_or_b32_e32 v192, 33, v159
	v_or_b32_e32 v193, 34, v159
	v_or_b32_e32 v194, 35, v159
	v_or_b32_e32 v195, 40, v159
	v_or_b32_e32 v196, 41, v159
	v_or_b32_e32 v197, 42, v159
	v_or_b32_e32 v198, 43, v159
	v_or_b32_e32 v199, 48, v159
	v_or_b32_e32 v200, 49, v159
	v_or_b32_e32 v201, 50, v159
	v_or_b32_e32 v202, 51, v159
	v_or_b32_e32 v203, 56, v159
	v_or_b32_e32 v204, 57, v159
	v_or_b32_e32 v205, 58, v159
	v_or_b32_e32 v206, 59, v159
	v_or_b32_e32 v208, s40, v29
	v_or_b32_e32 v209, s48, v6
	s_mov_b64 s[38:39], -1
	v_add_u32_e32 v211, 0x4000, v210
	v_add_u32_e32 v213, 0x4000, v212
	v_add_u32_e32 v214, s0, v10
	v_add_u32_e32 v215, s0, v13
	v_add_u32_e32 v216, s0, v15
	v_add_u32_e32 v217, s0, v17
	v_add_u32_e32 v218, s0, v19
	v_add_u32_e32 v219, s0, v21
	v_add_u32_e32 v220, s0, v23
	v_add_u32_e32 v221, s0, v25
	v_add_u32_e32 v222, s0, v4
	v_add_u32_e32 v223, s0, v5
	v_add_u32_e32 v224, s0, v7
	v_add_u32_e32 v225, s0, v9
	v_add_u32_e32 v226, s0, v11
	v_add_u32_e32 v227, s0, v12
	v_add_u32_e32 v228, s0, v14
	v_add_u32_e32 v229, s0, v8
	v_mov_b32_e32 v230, 0xf149f2ca
	v_mov_b32_e32 v231, 0x8000
	v_writelane_b32 v252, s49, 34
	v_writelane_b32 v252, s50, 35
	s_branch .LBB2_2

.LBB2_22:
	s_add_u32 s2, s81, s76
	s_addc_u32 s3, s94, s77
	s_add_i32 m0, s101, 0x2000
	s_add_u32 s36, s98, s76
	s_addc_u32 s37, s80, s77
	global_load_lds_dwordx4 v172, s[2:3]
	s_add_i32 m0, s101, 0x6000
	s_add_u32 s2, s2, 0x400
	s_addc_u32 s3, s3, 0
	global_load_lds_dwordx4 v173, s[36:37]
	s_add_i32 m0, s101, 0x2400
	s_add_u32 s36, s95, s76
	s_addc_u32 s37, s96, s77
	global_load_lds_dwordx4 v174, s[2:3]
	s_add_i32 m0, s101, 0x6400
	s_nop 0
	global_load_lds_dwordx4 v175, s[36:37]
.LBB2_23:
	s_add_i32 s79, s69, 2
	s_cmp_gt_u32 s79, s92
	s_cselect_b64 s[82:83], -1, 0
	s_cmp_le_u32 s79, s92
	s_cselect_b64 s[86:87], -1, 0
	s_and_b64 vcc, exec, s[82:83]
	s_cbranch_vccnz .LBB2_26
	v_readlane_b32 s2, v252, 36
	s_add_i32 s2, s2, s33
	s_ashr_i32 s2, s2, 5
	v_readlane_b32 s3, v252, 12
	s_add_i32 s2, s2, s3
	s_cmp_lt_i32 s2, -1
	s_cbranch_scc1 .LBB2_26
	s_lshl_b32 s36, s2, 12
	s_and_b32 s37, s36, 0x7000
	s_add_i32 s37, s37, s100
	s_and_b32 s3, s101, 0x1800
	s_or_b32 s3, s3, 0x1000
	s_add_i32 s36, s36, s3
	s_add_u32 s2, s74, s36
	s_addc_u32 s3, s75, 0
	s_add_i32 m0, s37, 0x8000
	s_add_i32 s36, s36, 0x400
	global_load_lds_dwordx4 v172, s[2:3]
	s_add_u32 s2, s74, s36
	s_addc_u32 s3, s75, 0
	s_add_i32 m0, s37, 0x8400
	s_nop 0
	global_load_lds_dwordx4 v174, s[2:3]

.LBB2_38:
	s_waitcnt vmcnt(0)
	s_andn2_b64 vcc, exec, s[84:85]
	s_waitcnt vmcnt(0) lgkmcnt(0)
	s_barrier
	s_cbranch_vccnz .LBB2_53
	s_andn2_b64 vcc, exec, s[86:87]
	s_cbranch_vccnz .LBB2_41
	s_add_u32 s36, s97, s76
	s_addc_u32 s37, s68, s77
	s_mov_b32 m0, s101
	s_nop 0
	global_load_lds_dwordx4 v172, s[36:37]
	s_add_u32 s36, s93, s76
	s_addc_u32 s37, s91, s77
	s_add_i32 m0, s101, 0x4000
	s_nop 0
	global_load_lds_dwordx4 v173, s[36:37]
	s_add_u32 s36, s90, s76
	s_addc_u32 s37, s99, s77
	s_add_i32 m0, s101, 0x400
	s_nop 0
	global_load_lds_dwordx4 v174, s[36:37]
	s_add_u32 s36, s0, s76
	s_addc_u32 s37, s1, s77
	s_add_i32 m0, s101, 0x4400
	s_nop 0
	global_load_lds_dwordx4 v175, s[36:37]
.LBB2_41:
	v_readlane_b32 s3, v252, 40
	s_cmp_gt_i32 s69, s3
	s_cbranch_scc1 .LBB2_44
	v_readlane_b32 s3, v252, 36
	s_add_i32 s3, s3, s33
	s_sub_i32 s3, s3, 64
	s_ashr_i32 s3, s3, 5
	v_readlane_b32 s36, v252, 12
	s_add_i32 s3, s3, s36
	s_cmp_lt_i32 s3, -1
	s_cbranch_scc1 .LBB2_44
	s_lshl_b32 s3, s3, 12
	s_and_b32 s38, s3, 0x7000
	s_add_i32 s38, s38, s100
	s_and_b32 s36, s101, 0x1800
	s_or_b32 s36, s36, 0x1000
	s_add_i32 s3, s3, s36
	s_add_u32 s36, s74, s3
	s_addc_u32 s37, s75, 0
	s_add_i32 m0, s38, 0x8000
	s_add_i32 s3, s3, 0x400
	global_load_lds_dwordx4 v172, s[36:37]
	s_add_u32 s36, s74, s3
	s_addc_u32 s37, s75, 0
	s_add_i32 m0, s38, 0x8400
	s_nop 0
	global_load_lds_dwordx4 v174, s[36:37]
